# baseline (speedup 1.0000x reference)
_Z16sum_layer_kernelPKfS0_Pf:
	s_load_dwordx4 s[4:7], s[0:1], 0x0
	s_load_dwordx2 s[8:9], s[0:1], 0x10
	v_lshrrev_b32_e32 v42, 6, v0
	v_bfe_u32 v41, v0, 5, 1
	v_and_b32_e32 v40, 31, v0
	v_readfirstlane_b32 s23, v42
	v_and_b32_e32 v43, 7, v0
	v_bfe_u32 v44, v0, 3, 3
	s_lshl_b32 s3, s2, 12
	s_lshl_b32 s19, s2, 7
	s_lshl_b32 s23, s23, 12
	v_lshlrev_b32_e32 v1, 11, v41
	v_lshl_or_b32 v1, v40, 2, v1
	s_mov_b32 m0, s23
	v_lshrrev_b32_e32 v46, 1, v44
	v_xor_b32_e32 v46, v43, v46
	v_lshlrev_b32_e32 v46, 4, v46
	v_lshl_add_u32 v35, v44, 16, v46
	v_lshl_add_u32 v35, v42, 21, v35
	v_add_u32_e32 v35, s19, v35
	v_xor_b32_e32 v86, 64, v35
	s_mov_b32 s20, 0x7fc00
	s_mov_b32 s21, 0xff800
	s_mov_b32 s22, 0x17f400
	s_mov_b32 s14, 0x200000
	s_mov_b32 s15, 0x20000
	s_waitcnt lgkmcnt(0)
	s_mov_b32 s12, s6
	s_and_b32 s13, s7, 0xffff
	s_and_b32 s5, s5, 0xffff
	s_mov_b32 s6, 0x800000
	s_mov_b32 s7, s15
	buffer_load_dword v18, v1, s[12:15], s3 offen nt
	buffer_load_dword v19, v1, s[12:15], s3 offen offset:128 nt
	buffer_load_dword v20, v1, s[12:15], s3 offen offset:256 nt
	buffer_load_dword v21, v1, s[12:15], s3 offen offset:384 nt
	buffer_load_dword v22, v1, s[12:15], s3 offen offset:512 nt
	buffer_load_dword v23, v1, s[12:15], s3 offen offset:640 nt
	buffer_load_dword v24, v1, s[12:15], s3 offen offset:768 nt
	buffer_load_dword v25, v1, s[12:15], s3 offen offset:896 nt
	buffer_load_dword v26, v1, s[12:15], s3 offen offset:1024 nt
	buffer_load_dword v27, v1, s[12:15], s3 offen offset:1152 nt
	buffer_load_dword v28, v1, s[12:15], s3 offen offset:1280 nt
	buffer_load_dword v29, v1, s[12:15], s3 offen offset:1408 nt
	buffer_load_dword v30, v1, s[12:15], s3 offen offset:1536 nt
	buffer_load_dword v31, v1, s[12:15], s3 offen offset:1664 nt
	buffer_load_dword v32, v1, s[12:15], s3 offen offset:1792 nt
	buffer_load_dword v33, v1, s[12:15], s3 offen offset:1920 nt
	buffer_load_dwordx4 v35, s[4:7], 0 offen nt lds
	buffer_load_dwordx4 v86, s[4:7], s20 offen offset:1024 nt lds
	buffer_load_dwordx4 v35, s[4:7], s21 offen offset:2048 nt lds
	buffer_load_dwordx4 v86, s[4:7], s22 offen offset:3072 nt lds
	v_and_b32_e32 v45, 63, v0
	v_lshlrev_b32_e32 v36, 2, v40
	v_lshl_add_u32 v36, v41, 18, v36
	v_lshl_add_u32 v36, v42, 21, v36
	v_add_u32_e32 v36, s19, v36
	v_bfe_u32 v47, v40, 1, 3
	v_lshlrev_b32_e32 v39, 2, v41
	v_xor_b32_e32 v39, v39, v47
	v_lshlrev_b32_e32 v39, 4, v39
	v_lshl_add_u32 v39, v40, 7, v39
	v_lshl_add_u32 v39, v42, 12, v39
	v_xor_b32_e32 v81, 16, v39
	v_xor_b32_e32 v82, 32, v39
	v_xor_b32_e32 v83, 48, v39
	v_cmp_gt_u32_e32 vcc, 32, v45
	v_mov_b32_e32 v34, 0xc1600000
	v_mov_b32_e32 v84, 0x3fb8aa3b
	v_mov_b32_e32 v85, 0x3f317218
	s_lshl_b32 s24, 1, 16
	s_lshl_b32 s25, 2, 16
	s_lshl_b32 s26, 3, 16
	s_lshl_b32 s27, 8, 16
	s_lshl_b32 s28, 9, 16
	s_lshl_b32 s29, 10, 16
	s_lshl_b32 s30, 11, 16
	s_lshl_b32 s31, 16, 16
	s_lshl_b32 s32, 17, 16
	s_lshl_b32 s33, 18, 16
	s_lshl_b32 s34, 19, 16
	s_lshl_b32 s35, 24, 16
	s_lshl_b32 s36, 25, 16
	s_lshl_b32 s37, 26, 16
	s_lshl_b32 s38, 27, 16
	s_and_b32 s9, s9, 0xffff
	s_mov_b32 s10, s6
	s_mov_b32 s11, s15
	s_waitcnt vmcnt(4)
	v_max3_f32 v48, v18, v19, v20
	v_max3_f32 v50, v21, v22, v23
	v_max3_f32 v48, v48, v24, v25
	v_max3_f32 v50, v50, v26, v27
	v_max3_f32 v48, v48, v28, v29
	v_max3_f32 v50, v50, v30, v31
	v_max3_f32 v48, v48, v32, v33
	v_max_f32_e32 v48, v48, v50
	v_mov_b32_e32 v50, v48
	s_nop 1
	v_permlane32_swap_b32_e32 v48, v50
	v_max_f32_e32 v48, v48, v50
	v_fmamk_f32 v48, v48, 0x3fb8aa3b, v34
	v_pk_fma_f32 v[18:19], v[18:19], v[84:85], v[48:49] op_sel_hi:[1,0,0] neg_lo:[0,0,1] neg_hi:[0,0,1]
	v_exp_f32_e32 v18, v18
	v_exp_f32_e32 v19, v19
	v_pk_fma_f32 v[20:21], v[20:21], v[84:85], v[48:49] op_sel_hi:[1,0,0] neg_lo:[0,0,1] neg_hi:[0,0,1]
	v_exp_f32_e32 v20, v20
	v_exp_f32_e32 v21, v21
	v_pk_fma_f32 v[22:23], v[22:23], v[84:85], v[48:49] op_sel_hi:[1,0,0] neg_lo:[0,0,1] neg_hi:[0,0,1]
	v_exp_f32_e32 v22, v22
	v_exp_f32_e32 v23, v23
	v_pk_fma_f32 v[24:25], v[24:25], v[84:85], v[48:49] op_sel_hi:[1,0,0] neg_lo:[0,0,1] neg_hi:[0,0,1]
	v_exp_f32_e32 v24, v24
	v_exp_f32_e32 v25, v25
	v_pk_fma_f32 v[26:27], v[26:27], v[84:85], v[48:49] op_sel_hi:[1,0,0] neg_lo:[0,0,1] neg_hi:[0,0,1]
	v_exp_f32_e32 v26, v26
	v_exp_f32_e32 v27, v27
	v_pk_fma_f32 v[28:29], v[28:29], v[84:85], v[48:49] op_sel_hi:[1,0,0] neg_lo:[0,0,1] neg_hi:[0,0,1]
	v_exp_f32_e32 v28, v28
	v_exp_f32_e32 v29, v29
	v_pk_fma_f32 v[30:31], v[30:31], v[84:85], v[48:49] op_sel_hi:[1,0,0] neg_lo:[0,0,1] neg_hi:[0,0,1]
	v_exp_f32_e32 v30, v30
	v_exp_f32_e32 v31, v31
	v_pk_fma_f32 v[32:33], v[32:33], v[84:85], v[48:49] op_sel_hi:[1,0,0] neg_lo:[0,0,1] neg_hi:[0,0,1]
	v_exp_f32_e32 v32, v32
	v_exp_f32_e32 v33, v33
	v_pk_add_f32 v[56:57], v[18:19], v[20:21]
	v_pk_add_f32 v[58:59], v[22:23], v[24:25]
	v_pk_add_f32 v[60:61], v[26:27], v[28:29]
	v_pk_add_f32 v[62:63], v[30:31], v[32:33]
	v_pk_add_f32 v[56:57], v[56:57], v[58:59]
	v_pk_add_f32 v[60:61], v[60:61], v[62:63]
	v_pk_add_f32 v[56:57], v[56:57], v[60:61]
	v_add_f32_e32 v50, v56, v57
	v_mov_b32_e32 v51, v50
	s_nop 1
	v_permlane32_swap_b32_e32 v50, v51
	v_add_f32_e32 v50, v50, v51
	v_log_f32_e32 v50, v50
	v_cvt_pk_f16_f32 v40, v18, v19
	v_cvt_pk_f16_f32 v41, v20, v21
	v_cvt_pk_f16_f32 v42, v22, v23
	v_cvt_pk_f16_f32 v43, v24, v25
	v_cvt_pk_f16_f32 v44, v26, v27
	v_cvt_pk_f16_f32 v45, v28, v29
	v_cvt_pk_f16_f32 v46, v30, v31
	v_cvt_pk_f16_f32 v47, v32, v33
	v_add_f32_e32 v50, 0x41600000, v50
	v_mul_f32_e32 v50, 0xbf317218, v50
	v_cndmask_b32_e64 v51, v50, 1.0, vcc
	s_waitcnt vmcnt(0)
	s_setprio 2
	ds_read_b128 v[2:5], v39
	ds_read_b128 v[6:9], v81
	ds_read_b128 v[10:13], v82
	ds_read_b128 v[14:17], v83
	s_waitcnt lgkmcnt(2)
	v_max3_f32 v52, v2, v3, v4
	v_max3_f32 v53, v5, v6, v7
	v_max_f32_e32 v52, v52, v8
	v_max_f32_e32 v53, v53, v9
	s_waitcnt lgkmcnt(0)
	v_max3_f32 v52, v52, v10, v11
	v_max3_f32 v53, v53, v12, v13
	v_max3_f32 v52, v52, v14, v15
	v_max3_f32 v53, v53, v16, v17
	v_max_f32_e32 v52, v52, v53
	v_mov_b32_e32 v53, v52
	s_nop 1
	v_permlane32_swap_b32_e32 v52, v53
	v_max_f32_e32 v52, v52, v53
	v_cndmask_b32_e32 v54, 1.0, v52, vcc
	v_fmamk_f32 v48, v52, 0x3fb8aa3b, v34
	v_pk_fma_f32 v[2:3], v[2:3], v[84:85], v[48:49] op_sel_hi:[1,0,0] neg_lo:[0,0,1] neg_hi:[0,0,1]
	v_mfma_f32_32x32x2_f32 v[64:79], v54, v51, 0
	v_exp_f32_e32 v2, v2
	v_exp_f32_e32 v3, v3
	v_pk_fma_f32 v[4:5], v[4:5], v[84:85], v[48:49] op_sel_hi:[1,0,0] neg_lo:[0,0,1] neg_hi:[0,0,1]
	v_exp_f32_e32 v4, v4
	v_exp_f32_e32 v5, v5
	v_pk_fma_f32 v[6:7], v[6:7], v[84:85], v[48:49] op_sel_hi:[1,0,0] neg_lo:[0,0,1] neg_hi:[0,0,1]
	v_exp_f32_e32 v6, v6
	v_exp_f32_e32 v7, v7
	v_pk_fma_f32 v[8:9], v[8:9], v[84:85], v[48:49] op_sel_hi:[1,0,0] neg_lo:[0,0,1] neg_hi:[0,0,1]
	v_exp_f32_e32 v8, v8
	v_exp_f32_e32 v9, v9
	v_pk_fma_f32 v[10:11], v[10:11], v[84:85], v[48:49] op_sel_hi:[1,0,0] neg_lo:[0,0,1] neg_hi:[0,0,1]
	v_exp_f32_e32 v10, v10
	v_cvt_pk_f16_f32 v56, v2, v3
	v_cvt_pk_f16_f32 v57, v4, v5
	v_cvt_pk_f16_f32 v58, v6, v7
	v_cvt_pk_f16_f32 v59, v8, v9
	v_exp_f32_e32 v11, v11
	v_pk_fma_f32 v[12:13], v[12:13], v[84:85], v[48:49] op_sel_hi:[1,0,0] neg_lo:[0,0,1] neg_hi:[0,0,1]
	v_exp_f32_e32 v12, v12
	v_mfma_f32_32x32x16_f16 v[18:33], v[56:59], v[40:43], 0
	v_exp_f32_e32 v13, v13
	v_pk_fma_f32 v[14:15], v[14:15], v[84:85], v[48:49] op_sel_hi:[1,0,0] neg_lo:[0,0,1] neg_hi:[0,0,1]
	v_exp_f32_e32 v14, v14
	v_exp_f32_e32 v15, v15
	v_pk_fma_f32 v[16:17], v[16:17], v[84:85], v[48:49] op_sel_hi:[1,0,0] neg_lo:[0,0,1] neg_hi:[0,0,1]
	v_exp_f32_e32 v16, v16
	v_exp_f32_e32 v17, v17
	v_cvt_pk_f16_f32 v60, v10, v11
	v_cvt_pk_f16_f32 v61, v12, v13
	v_cvt_pk_f16_f32 v62, v14, v15
	v_cvt_pk_f16_f32 v63, v16, v17
	s_nop 1
	v_mfma_f32_32x32x16_f16 v[18:33], v[60:63], v[44:47], v[18:33]
	s_nop 11
	v_log_f32_e32 v18, v18
	v_log_f32_e32 v19, v19
	v_log_f32_e32 v20, v20
	v_log_f32_e32 v21, v21
	v_log_f32_e32 v22, v22
	v_log_f32_e32 v23, v23
	v_pk_fma_f32 v[64:65], v[18:19], v[84:85], v[64:65] op_sel:[0,1,0] op_sel_hi:[1,1,1]
	buffer_store_dword v64, v36, s[8:11], 0 offen
	buffer_store_dword v65, v36, s[8:11], s24 offen
	v_log_f32_e32 v24, v24
	v_log_f32_e32 v25, v25
	v_pk_fma_f32 v[66:67], v[20:21], v[84:85], v[66:67] op_sel:[0,1,0] op_sel_hi:[1,1,1]
	buffer_store_dword v66, v36, s[8:11], s25 offen
	buffer_store_dword v67, v36, s[8:11], s26 offen
	v_log_f32_e32 v26, v26
	v_log_f32_e32 v27, v27
	v_pk_fma_f32 v[68:69], v[22:23], v[84:85], v[68:69] op_sel:[0,1,0] op_sel_hi:[1,1,1]
	buffer_store_dword v68, v36, s[8:11], s27 offen
	buffer_store_dword v69, v36, s[8:11], s28 offen
	v_log_f32_e32 v28, v28
	v_log_f32_e32 v29, v29
	v_pk_fma_f32 v[70:71], v[24:25], v[84:85], v[70:71] op_sel:[0,1,0] op_sel_hi:[1,1,1]
	buffer_store_dword v70, v36, s[8:11], s29 offen
	buffer_store_dword v71, v36, s[8:11], s30 offen
	v_log_f32_e32 v30, v30
	v_log_f32_e32 v31, v31
	v_pk_fma_f32 v[72:73], v[26:27], v[84:85], v[72:73] op_sel:[0,1,0] op_sel_hi:[1,1,1]
	buffer_store_dword v72, v36, s[8:11], s31 offen
	buffer_store_dword v73, v36, s[8:11], s32 offen
	v_log_f32_e32 v32, v32
	v_log_f32_e32 v33, v33
	v_pk_fma_f32 v[74:75], v[28:29], v[84:85], v[74:75] op_sel:[0,1,0] op_sel_hi:[1,1,1]
	buffer_store_dword v74, v36, s[8:11], s33 offen
	buffer_store_dword v75, v36, s[8:11], s34 offen
	v_pk_fma_f32 v[76:77], v[30:31], v[84:85], v[76:77] op_sel:[0,1,0] op_sel_hi:[1,1,1]
	buffer_store_dword v76, v36, s[8:11], s35 offen
	buffer_store_dword v77, v36, s[8:11], s36 offen
	v_pk_fma_f32 v[78:79], v[32:33], v[84:85], v[78:79] op_sel:[0,1,0] op_sel_hi:[1,1,1]
	buffer_store_dword v78, v36, s[8:11], s37 offen
	buffer_store_dword v79, v36, s[8:11], s38 offen
	s_endpgm
